# P5 proj epilogue: all gate bytes of the tile fetched in one batch instead of 16-32 dependent round trips
# baseline (speedup 1.0000x reference)
.LBB0_211:
	v_readfirstlane_b32 s38, v0
	s_lshr_b32 s10, s38, 6
	s_lshl_b32 s36, s3, 3
	s_cmpk_lg_i32 s3, 0x100
	s_cselect_b64 s[4:5], -1, 0
	s_cmpk_eq_i32 s3, 0x100
	s_cselect_b64 s[6:7], -1, 0
	s_lshl_b32 s8, s2, 3
	s_add_i32 s37, s10, s8
	s_cmp_lt_i32 s37, 0x12000
	s_cselect_b64 s[8:9], -1, 0
	s_or_b64 s[6:7], s[6:7], s[8:9]
	s_and_b64 s[6:7], s[6:7], exec
	s_cselect_b32 s11, s37, -1
	v_and_b32_e32 v2, 56, v0
	s_cmp_lt_i32 s11, 0
	s_barrier
	s_cbranch_scc1 .LBB0_237
	s_cmpk_gt_u32 s11, 0xbfff
	s_cbranch_scc0 .LBB0_214
	s_add_i32 s6, s11, 0xffff4000
	s_lshr_b32 s7, s6, 7
	s_mul_hi_u32 s8, s7, 0x55555556
	s_mul_i32 s8, s8, 3
	s_mul_hi_u32 s6, s6, 0xaaaaaaab
	s_sub_i32 s22, s7, s8
	s_lshr_b32 s8, s6, 8
	s_load_dwordx2 s[6:7], s[0:1], 0xa0
	s_load_dwordx2 s[20:21], s[0:1], 0xb0
	s_mul_i32 s24, s8, 0x600000
	s_mul_hi_u32 s23, s8, 0x600000
	s_mov_b32 s9, 0
	s_waitcnt lgkmcnt(0)
	s_add_u32 s6, s6, s24
	s_addc_u32 s7, s7, s23
	s_lshl_b32 s23, s11, 6
	s_lshl_b32 s22, s22, 8
	s_and_b32 s23, s23, 0xc0
	s_or_b32 s22, s22, s23
	s_lshl_b32 s23, s22, 13
	s_add_u32 s6, s6, s23
	s_addc_u32 s7, s7, 0
	s_lshl_b32 s23, s11, 4
	s_and_b32 s23, s23, 0x7c0
	s_lshl_b32 s24, s23, 2
	s_add_u32 s6, s6, s24
	s_addc_u32 s7, s7, 0
	s_lshl_b64 s[8:9], s[8:9], 11
	s_or_b32 s8, s8, s23
	s_mul_i32 s23, s8, 0x300
	s_mul_hi_u32 s8, s8, 0x300
	s_mulk_i32 s9, 0x300
	s_add_i32 s8, s8, s9
	s_add_u32 s9, s20, s23
	s_addc_u32 s8, s21, s8
	s_add_u32 s9, s9, s22
	s_addc_u32 s8, s8, 0
	s_add_u32 s24, s9, 0x1b80a000
	s_addc_u32 s25, s8, 0
	s_mov_b64 s[8:9], 0
	s_branch .LBB0_215

.LBB0_217:
	v_and_b32_e32 v4, 28, v179
	s_lshl_b32 s8, s10, 14
	s_waitcnt vmcnt(6)
	v_mov_b32_e32 v7, 0
	v_lshlrev_b32_e32 v6, 2, v4
	v_mul_u32_u24_e32 v3, s34, v2
	s_add_i32 s39, s8, 0
	v_lshl_add_u64 v[8:9], s[6:7], 0, v[6:7]
	s_waitcnt vmcnt(5)
	v_lshlrev_b32_e32 v10, 2, v3
	v_mov_b32_e32 v11, v7
	s_mov_b32 s9, 0
	v_lshl_add_u64 v[12:13], v[8:9], 0, v[10:11]
	s_mov_b32 m0, s39
	s_lshl_b32 s8, s34, 2
	s_add_i32 s53, s39, 0x400
	s_add_i32 s10, s34, s34
	global_load_lds_dwordx4 v[12:13], off
	v_lshl_add_u64 v[12:13], v[12:13], 0, s[8:9]
	s_mov_b32 m0, s53
	s_add_i32 s54, s39, 0x800
	s_add_i32 s10, s10, s10
	global_load_lds_dwordx4 v[12:13], off
	v_lshl_add_u64 v[12:13], v[12:13], 0, s[8:9]
	s_mov_b32 m0, s54
	s_add_i32 s55, s39, 0xc00
	v_mov_b32_e32 v3, s10
	global_load_lds_dwordx4 v[12:13], off
	v_lshl_add_u64 v[12:13], v[12:13], 0, s[8:9]
	s_mov_b32 m0, s55
	v_mad_u32_u24 v3, s34, v2, v3
	global_load_lds_dwordx4 v[12:13], off
	v_lshlrev_b32_e32 v12, 2, v3
	v_mov_b32_e32 v13, v7
	s_add_i32 s56, s39, 0x1000
	s_waitcnt vmcnt(0)
	v_lshl_add_u64 v[14:15], v[8:9], 0, v[12:13]
	s_mov_b32 m0, s56
	v_add_u32_e32 v3, s34, v3
	global_load_lds_dwordx4 v[14:15], off
	v_lshlrev_b32_e32 v14, 2, v3
	v_mov_b32_e32 v15, v7
	s_add_i32 s57, s39, 0x1400
	v_lshl_add_u64 v[16:17], v[8:9], 0, v[14:15]
	s_mov_b32 m0, s57
	v_add_u32_e32 v3, s34, v3
	global_load_lds_dwordx4 v[16:17], off
	v_lshlrev_b32_e32 v16, 2, v3
	v_mov_b32_e32 v17, v7
	s_add_i32 s58, s39, 0x1800
	v_lshl_add_u64 v[18:19], v[8:9], 0, v[16:17]
	s_mov_b32 m0, s58
	s_add_i32 s59, s39, 0x1c00
	global_load_lds_dwordx4 v[18:19], off
	v_add_u32_e32 v18, s34, v3
	v_mov_b32_e32 v19, v7
	v_lshlrev_b64 v[18:19], 2, v[18:19]
	v_lshl_add_u64 v[8:9], v[8:9], 0, v[18:19]
	s_mov_b32 m0, s59
	s_add_i32 s60, s39, 0x2000
	global_load_lds_dwordx4 v[8:9], off
	v_lshl_add_u64 v[8:9], s[6:7], 0, v[10:11]
	v_lshl_add_u64 v[10:11], v[8:9], 0, v[6:7]
	s_mov_b64 s[10:11], 0x80
	v_lshl_add_u64 v[10:11], v[10:11], 0, s[10:11]
	s_mov_b32 m0, s60
	v_lshl_add_u64 v[8:9], v[8:9], 0, s[8:9]
	global_load_lds_dwordx4 v[10:11], off
	v_lshl_add_u64 v[10:11], v[8:9], 0, v[6:7]
	s_add_i32 s62, s39, 0x2400
	v_lshl_add_u64 v[10:11], v[10:11], 0, s[10:11]
	s_mov_b32 m0, s62
	v_lshl_add_u64 v[8:9], v[8:9], 0, s[8:9]
	global_load_lds_dwordx4 v[10:11], off
	v_lshl_add_u64 v[10:11], v[8:9], 0, v[6:7]
	s_add_i32 s64, s39, 0x2800
	v_lshl_add_u64 v[8:9], v[8:9], 0, s[8:9]
	v_lshl_add_u64 v[10:11], v[10:11], 0, s[10:11]
	s_mov_b32 m0, s64
	v_lshl_add_u64 v[8:9], v[8:9], 0, v[6:7]
	s_add_i32 s65, s39, 0x2c00
	global_load_lds_dwordx4 v[10:11], off
	v_lshl_add_u64 v[8:9], v[8:9], 0, s[10:11]
	s_mov_b32 m0, s65
	s_add_i32 s66, s39, 0x3000
	global_load_lds_dwordx4 v[8:9], off
	v_lshl_add_u64 v[8:9], s[6:7], 0, v[12:13]
	v_lshl_add_u64 v[8:9], v[8:9], 0, v[6:7]
	v_lshl_add_u64 v[8:9], v[8:9], 0, s[10:11]
	s_mov_b32 m0, s66
	s_add_i32 s67, s39, 0x3400
	global_load_lds_dwordx4 v[8:9], off
	v_lshl_add_u64 v[8:9], s[6:7], 0, v[14:15]
	v_lshl_add_u64 v[8:9], v[8:9], 0, v[6:7]
	v_lshl_add_u64 v[8:9], v[8:9], 0, s[10:11]
	s_mov_b32 m0, s67
	s_add_i32 s68, s39, 0x3800
	global_load_lds_dwordx4 v[8:9], off
	v_lshl_add_u64 v[8:9], s[6:7], 0, v[16:17]
	v_lshl_add_u64 v[8:9], v[8:9], 0, v[6:7]
	v_lshl_add_u64 v[8:9], v[8:9], 0, s[10:11]
	s_mov_b32 m0, s68
	s_add_i32 s69, s39, 0x3c00
	global_load_lds_dwordx4 v[8:9], off
	v_lshl_add_u64 v[8:9], s[6:7], 0, v[18:19]
	v_lshl_add_u64 v[8:9], v[8:9], 0, v[6:7]
	v_lshl_add_u64 v[8:9], v[8:9], 0, s[10:11]
	s_mov_b32 m0, s69
	s_cmpk_gt_i32 s2, 0x7f
	global_load_lds_dwordx4 v[8:9], off
	s_load_dwordx2 s[22:23], s[0:1], 0xa0
	s_load_dwordx2 s[26:27], s[0:1], 0xb0
	s_cselect_b64 s[20:21], -1, 0
	v_and_b32_e32 v5, 0x3f0, v180
	v_or_b32_e32 v8, 1, v2
	v_or_b32_e32 v10, 2, v2
	s_waitcnt lgkmcnt(0)
	s_add_u32 s70, s26, 0x1b80a000
	s_addc_u32 s71, s27, 0
	s_add_u32 s72, s26, 0x380a000
	v_or_b32_e32 v12, 3, v2
	v_or_b32_e32 v14, 4, v2
	v_or_b32_e32 v16, 5, v2
	v_or_b32_e32 v18, 6, v2
	v_or_b32_e32 v20, 7, v2
	v_mov_b32_e32 v3, v7
	v_or_b32_e32 v22, 32, v4
	v_or_b32_e32 v24, 1, v4
	v_or_b32_e32 v26, 2, v4
	v_or_b32_e32 v28, 3, v4
	v_or_b32_e32 v30, 33, v4
	v_or_b32_e32 v32, 34, v4
	v_or_b32_e32 v34, 35, v4
	s_addc_u32 s73, s27, 0
	s_add_i32 s75, s37, 0x8800
	s_add_i32 s76, s37, 0x800
	s_add_i32 s77, s37, s36
	s_movk_i32 s74, 0x90
	v_add_u32_e32 v5, s39, v5
	s_mov_b32 s78, 0
	s_branch .LBB0_221
.LBB0_218:
	ds_read_b128 v[38:41], v5 offset:8192
	ds_read_b128 v[42:45], v5 offset:9216
	ds_read_b128 v[46:49], v5 offset:10240
	ds_read_b128 v[50:53], v5 offset:11264
	ds_read_b128 v[54:57], v5 offset:12288
	ds_read_b128 v[58:61], v5 offset:13312
	ds_read_b128 v[62:65], v5 offset:14336
	ds_read_b128 v[66:69], v5 offset:15360
	s_waitcnt lgkmcnt(0)
	v_mul_f32_e32 v9, s63, v38
	v_mul_f32_e32 v11, s63, v42
	v_mov_b32_e32 v70, 0
	v_cvt_pk_fp8_f32 v70, v9, v11
	v_mul_f32_e32 v13, s63, v54
	v_mul_f32_e32 v15, s63, v58
	v_mov_b32_e32 v71, 0
	v_cvt_pk_fp8_f32 v71, v13, v15
	v_mul_f32_e32 v9, s63, v46
	v_mul_f32_e32 v11, s63, v50
	v_cvt_pk_fp8_f32 v70, v9, v11 op_sel:[0,0,1]
	v_mul_f32_e32 v9, s63, v62
	v_mul_f32_e32 v11, s63, v66
	v_cvt_pk_fp8_f32 v71, v9, v11 op_sel:[0,0,1]
	v_mul_f32_e32 v9, s63, v39
	v_mul_f32_e32 v11, s63, v43
	v_mov_b32_e32 v38, 0
	v_cvt_pk_fp8_f32 v38, v9, v11
	v_mul_f32_e32 v13, s63, v55
	v_mul_f32_e32 v15, s63, v59
	v_mov_b32_e32 v39, 0
	v_cvt_pk_fp8_f32 v39, v13, v15
	v_mul_f32_e32 v9, s63, v47
	v_mul_f32_e32 v11, s63, v51
	v_cvt_pk_fp8_f32 v38, v9, v11 op_sel:[0,0,1]
	v_mul_f32_e32 v9, s63, v63
	v_mul_f32_e32 v11, s63, v67
	v_cvt_pk_fp8_f32 v39, v9, v11 op_sel:[0,0,1]
	v_mad_u64_u32 v[72:73], s[24:25], s61, v22, v[36:37]
	v_mad_u64_u32 v[42:43], s[24:25], s61, v30, v[36:37]
	global_store_dwordx2 v[72:73], v[70:71], off
	global_store_dwordx2 v[42:43], v[38:39], off
	v_mul_f32_e32 v9, s63, v40
	v_mul_f32_e32 v11, s63, v44
	v_mov_b32_e32 v38, 0
	v_cvt_pk_fp8_f32 v38, v9, v11
	v_mul_f32_e32 v13, s63, v56
	v_mul_f32_e32 v15, s63, v60
	v_mov_b32_e32 v39, 0
	v_cvt_pk_fp8_f32 v39, v13, v15
	v_mul_f32_e32 v9, s63, v48
	v_mul_f32_e32 v11, s63, v52
	v_cvt_pk_fp8_f32 v38, v9, v11 op_sel:[0,0,1]
	v_mul_f32_e32 v9, s63, v64
	v_mul_f32_e32 v11, s63, v68
	v_cvt_pk_fp8_f32 v39, v9, v11 op_sel:[0,0,1]
	v_mul_f32_e32 v9, s63, v41
	v_mul_f32_e32 v11, s63, v45
	v_mov_b32_e32 v40, 0
	v_cvt_pk_fp8_f32 v40, v9, v11
	v_mul_f32_e32 v13, s63, v57
	v_mul_f32_e32 v15, s63, v61
	v_mov_b32_e32 v41, 0
	v_cvt_pk_fp8_f32 v41, v13, v15
	v_mul_f32_e32 v9, s63, v49
	v_mul_f32_e32 v11, s63, v53
	v_cvt_pk_fp8_f32 v40, v9, v11 op_sel:[0,0,1]
	v_mul_f32_e32 v9, s63, v65
	v_mul_f32_e32 v11, s63, v69
	v_cvt_pk_fp8_f32 v41, v9, v11 op_sel:[0,0,1]
	v_mad_u64_u32 v[42:43], s[24:25], s61, v32, v[36:37]
	v_mad_u64_u32 v[36:37], s[24:25], s61, v34, v[36:37]
	global_store_dwordx2 v[42:43], v[38:39], off
	global_store_dwordx2 v[36:37], v[40:41], off
	s_waitcnt lgkmcnt(0)
	s_andn2_b64 vcc, exec, s[28:29]
	s_cbranch_vccnz .LBB0_231
	v_mad_u64_u32 v[36:37], s[24:25], s34, v2, 0
	v_lshl_add_u64 v[36:37], v[36:37], 2, s[6:7]
	v_lshl_add_u64 v[36:37], v[36:37], 0, v[6:7]
	s_mov_b32 m0, s60
	v_lshl_add_u64 v[36:37], v[36:37], 0, s[10:11]
	global_load_lds_dwordx4 v[36:37], off
	v_mad_u64_u32 v[36:37], s[24:25], s34, v8, 0
	v_lshl_add_u64 v[36:37], v[36:37], 2, s[6:7]
	v_lshl_add_u64 v[36:37], v[36:37], 0, v[6:7]
	v_lshl_add_u64 v[36:37], v[36:37], 0, s[10:11]
	s_mov_b32 m0, s62
	s_addk_i32 s75, 0x400
	global_load_lds_dwordx4 v[36:37], off
	v_mad_u64_u32 v[36:37], s[24:25], s34, v10, 0
	v_lshl_add_u64 v[36:37], v[36:37], 2, s[6:7]
	v_lshl_add_u64 v[36:37], v[36:37], 0, v[6:7]
	v_lshl_add_u64 v[36:37], v[36:37], 0, s[10:11]
	s_mov_b32 m0, s64
	s_addk_i32 s76, 0x800
	global_load_lds_dwordx4 v[36:37], off
	v_mad_u64_u32 v[36:37], s[24:25], s34, v12, 0
	v_lshl_add_u64 v[36:37], v[36:37], 2, s[6:7]
	v_lshl_add_u64 v[36:37], v[36:37], 0, v[6:7]
	v_lshl_add_u64 v[36:37], v[36:37], 0, s[10:11]
	s_mov_b32 m0, s65
	s_add_i32 s77, s77, s36
	global_load_lds_dwordx4 v[36:37], off
	v_mad_u64_u32 v[36:37], s[24:25], s34, v14, 0
	v_lshl_add_u64 v[36:37], v[36:37], 2, s[6:7]
	v_lshl_add_u64 v[36:37], v[36:37], 0, v[6:7]
	v_lshl_add_u64 v[36:37], v[36:37], 0, s[10:11]
	s_mov_b32 m0, s66
	s_add_i32 s78, s78, 1
	global_load_lds_dwordx4 v[36:37], off
	v_mad_u64_u32 v[36:37], s[24:25], s34, v16, 0
	v_lshl_add_u64 v[36:37], v[36:37], 2, s[6:7]
	v_lshl_add_u64 v[36:37], v[36:37], 0, v[6:7]
	v_lshl_add_u64 v[36:37], v[36:37], 0, s[10:11]
	s_mov_b32 m0, s67
	s_nop 0
	global_load_lds_dwordx4 v[36:37], off
	v_mad_u64_u32 v[36:37], s[24:25], s34, v18, 0
	v_lshl_add_u64 v[36:37], v[36:37], 2, s[6:7]
	v_lshl_add_u64 v[36:37], v[36:37], 0, v[6:7]
	v_lshl_add_u64 v[36:37], v[36:37], 0, s[10:11]
	s_mov_b32 m0, s68
	s_nop 0
	global_load_lds_dwordx4 v[36:37], off
	v_mad_u64_u32 v[36:37], s[24:25], s34, v20, 0
	v_lshl_add_u64 v[36:37], v[36:37], 2, s[6:7]
	v_lshl_add_u64 v[36:37], v[36:37], 0, v[6:7]
	v_lshl_add_u64 v[36:37], v[36:37], 0, s[10:11]
	s_mov_b32 m0, s69
	s_mov_b64 s[24:25], 0
	global_load_lds_dwordx4 v[36:37], off

.LBB0_231:
	s_mov_b64 s[24:25], -1
	s_branch .LBB0_220

.LBB0_233:
	s_waitcnt vmcnt(8)
	ds_read_b128 v[38:41], v5
	ds_read_b128 v[42:45], v5 offset:1024
	ds_read_b128 v[46:49], v5 offset:2048
	ds_read_b128 v[50:53], v5 offset:3072
	ds_read_b128 v[54:57], v5 offset:4096
	ds_read_b128 v[58:61], v5 offset:5120
	ds_read_b128 v[62:65], v5 offset:6144
	ds_read_b128 v[66:69], v5 offset:7168
	s_waitcnt lgkmcnt(0)
	v_mul_f32_e32 v6, s63, v38
	v_mul_f32_e32 v9, s63, v42
	v_mov_b32_e32 v70, 0
	v_cvt_pk_fp8_f32 v70, v6, v9
	v_mul_f32_e32 v11, s63, v54
	v_mul_f32_e32 v13, s63, v58
	v_mov_b32_e32 v71, 0
	v_cvt_pk_fp8_f32 v71, v11, v13
	v_mul_f32_e32 v6, s63, v46
	v_mul_f32_e32 v9, s63, v50
	v_cvt_pk_fp8_f32 v70, v6, v9 op_sel:[0,0,1]
	v_mul_f32_e32 v6, s63, v62
	v_mul_f32_e32 v9, s63, v66
	v_cvt_pk_fp8_f32 v71, v6, v9 op_sel:[0,0,1]
	v_mul_f32_e32 v6, s63, v39
	v_mul_f32_e32 v9, s63, v43
	v_mov_b32_e32 v38, 0
	v_cvt_pk_fp8_f32 v38, v6, v9
	v_mul_f32_e32 v11, s63, v55
	v_mul_f32_e32 v13, s63, v59
	v_mov_b32_e32 v39, 0
	v_cvt_pk_fp8_f32 v39, v11, v13
	v_mul_f32_e32 v6, s63, v47
	v_mul_f32_e32 v9, s63, v51
	v_cvt_pk_fp8_f32 v38, v6, v9 op_sel:[0,0,1]
	v_mul_f32_e32 v6, s63, v63
	v_mul_f32_e32 v9, s63, v67
	v_cvt_pk_fp8_f32 v39, v6, v9 op_sel:[0,0,1]
	v_lshl_add_u64 v[36:37], s[24:25], 0, v[2:3]
	v_mad_u64_u32 v[72:73], s[24:25], s61, v4, v[36:37]
	v_mad_u64_u32 v[42:43], s[24:25], s61, v24, v[36:37]
	global_store_dwordx2 v[72:73], v[70:71], off
	global_store_dwordx2 v[42:43], v[38:39], off
	v_mul_f32_e32 v6, s63, v40
	v_mul_f32_e32 v9, s63, v44
	v_mov_b32_e32 v38, 0
	v_cvt_pk_fp8_f32 v38, v6, v9
	v_mul_f32_e32 v11, s63, v56
	v_mul_f32_e32 v13, s63, v60
	v_mov_b32_e32 v39, 0
	v_cvt_pk_fp8_f32 v39, v11, v13
	v_mul_f32_e32 v6, s63, v48
	v_mul_f32_e32 v9, s63, v52
	v_cvt_pk_fp8_f32 v38, v6, v9 op_sel:[0,0,1]
	v_mul_f32_e32 v6, s63, v64
	v_mul_f32_e32 v9, s63, v68
	v_cvt_pk_fp8_f32 v39, v6, v9 op_sel:[0,0,1]
	v_mul_f32_e32 v6, s63, v41
	v_mul_f32_e32 v9, s63, v45
	v_mov_b32_e32 v40, 0
	v_cvt_pk_fp8_f32 v40, v6, v9
	v_mul_f32_e32 v11, s63, v57
	v_mul_f32_e32 v13, s63, v61
	v_mov_b32_e32 v41, 0
	v_cvt_pk_fp8_f32 v41, v11, v13
	v_mul_f32_e32 v6, s63, v49
	v_mul_f32_e32 v9, s63, v53
	v_cvt_pk_fp8_f32 v40, v6, v9 op_sel:[0,0,1]
	v_mul_f32_e32 v6, s63, v65
	v_mul_f32_e32 v9, s63, v69
	v_cvt_pk_fp8_f32 v41, v6, v9 op_sel:[0,0,1]
	v_mad_u64_u32 v[42:43], s[24:25], s61, v26, v[36:37]
	global_store_dwordx2 v[42:43], v[38:39], off
	v_mad_u64_u32 v[38:39], s[24:25], s61, v28, v[36:37]
	global_store_dwordx2 v[38:39], v[40:41], off
	s_waitcnt lgkmcnt(0)
	s_mov_b64 s[24:25], -1
	s_and_b64 vcc, exec, s[30:31]
	s_cbranch_vccz .LBB0_235
	s_waitcnt vmcnt(0)
	s_mov_b64 s[24:25], 0
.LBB0_235:
	s_andn2_b64 vcc, exec, s[24:25]
	v_lshlrev_b32_e32 v6, 2, v4
	s_cbranch_vccnz .LBB0_218
	v_lshl_add_u64 v[38:39], s[6:7], 0, v[6:7]
	v_mad_u64_u32 v[40:41], s[24:25], s34, v2, 0
	s_mov_b32 m0, s39
	v_lshl_add_u64 v[40:41], v[40:41], 2, v[38:39]
	global_load_lds_dwordx4 v[40:41], off
	v_mad_u64_u32 v[40:41], s[24:25], s34, v8, 0
	v_lshl_add_u64 v[40:41], v[40:41], 2, v[38:39]
	s_mov_b32 m0, s53
	s_nop 0
	global_load_lds_dwordx4 v[40:41], off
	v_mad_u64_u32 v[40:41], s[24:25], s34, v10, 0
	v_lshl_add_u64 v[40:41], v[40:41], 2, v[38:39]
	s_mov_b32 m0, s54
	s_nop 0
	global_load_lds_dwordx4 v[40:41], off
	v_mad_u64_u32 v[40:41], s[24:25], s34, v12, 0
	v_lshl_add_u64 v[40:41], v[40:41], 2, v[38:39]
	s_mov_b32 m0, s55
	s_nop 0
	global_load_lds_dwordx4 v[40:41], off
	v_mad_u64_u32 v[40:41], s[24:25], s34, v14, 0
	v_lshl_add_u64 v[40:41], v[40:41], 2, v[38:39]
	s_mov_b32 m0, s56
	s_nop 0
	global_load_lds_dwordx4 v[40:41], off
	v_mad_u64_u32 v[40:41], s[24:25], s34, v16, 0
	v_lshl_add_u64 v[40:41], v[40:41], 2, v[38:39]
	s_mov_b32 m0, s57
	s_nop 0
	global_load_lds_dwordx4 v[40:41], off
	v_mad_u64_u32 v[40:41], s[24:25], s34, v18, 0
	v_lshl_add_u64 v[40:41], v[40:41], 2, v[38:39]
	s_mov_b32 m0, s58
	s_nop 0
	global_load_lds_dwordx4 v[40:41], off
	v_mad_u64_u32 v[40:41], s[24:25], s34, v20, 0
	v_lshl_add_u64 v[38:39], v[40:41], 2, v[38:39]
	s_mov_b32 m0, s59
	s_nop 0
	global_load_lds_dwordx4 v[38:39], off
	s_waitcnt vmcnt(8)
	s_branch .LBB0_218
.LBB0_237:
	s_waitcnt vmcnt(0)
	s_load_dwordx2 s[4:5], s[0:1], 0xb0
	s_cmpk_gt_i32 s37, 0x7ff
	s_cbranch_scc1 .LBB0_245
	s_load_dwordx2 s[6:7], s[0:1], 0x60
	s_waitcnt vmcnt(0)
	v_and_b32_e32 v10, 28, v179
	s_bfe_u32 s20, s38, 0x30006
	v_mov_b32_e32 v5, 0
	v_lshlrev_b32_e32 v8, 11, v10
	v_lshlrev_b32_e32 v12, 10, v10
	s_waitcnt lgkmcnt(0)
	s_add_u32 s21, s4, 0x300a000
	v_lshlrev_b32_e32 v4, 2, v10
	s_addc_u32 s22, s5, 0
	v_lshl_add_u64 v[6:7], s[6:7], 0, v[4:5]
	s_mov_b32 s7, 0
	s_movk_i32 s23, 0x1000
	s_movk_i32 s24, 0x2000
	s_movk_i32 s25, 0x3000
	s_mov_b64 s[8:9], 0x80
	v_lshlrev_b32_e32 v8, 1, v8
	s_mov_b32 s26, 0x21000
	s_mov_b32 s27, 0x22000
	s_mov_b32 s28, 0x280a000
	v_lshlrev_b32_e32 v4, 2, v10
	v_lshlrev_b32_e32 v10, 1, v12
	s_mov_b32 s29, 0x10000
	s_mov_b32 s30, 0x11000
	v_lshlrev_b32_e32 v12, 1, v2
	s_branch .LBB0_240

.LBB0_701:
	v_lshl_add_u32 v152, s30, 8, v1
	v_mov_b64_e32 v[150:151], s[12:13]
	v_lshl_or_b32 v4, s34, 8, v161
	v_mad_i64_i32 v[154:155], s[6:7], v152, s63, v[150:151]
	v_lshl_add_u64 v[158:159], v[154:155], 0, s[20:21]
	v_ashrrev_i32_e32 v5, 31, v4
	v_lshl_add_u64 v[150:151], v[158:159], 0, v[4:5]
	v_mad_u32_u24 v246, v152, s63, v4
	s_add_u32 s80, s12, 0x3400
	s_addc_u32 s81, s13, 0
	global_load_dwordx2 v[182:183], v246, s[80:81]
	global_load_dwordx2 v[184:185], v246, s[80:81] offset:128
	s_add_u32 s80, s12, 0x4f400
	s_addc_u32 s81, s13, 0
	global_load_dwordx2 v[186:187], v246, s[80:81]
	global_load_dwordx2 v[188:189], v246, s[80:81] offset:128
	s_add_u32 s80, s12, 0x9b400
	s_addc_u32 s81, s13, 0
	global_load_dwordx2 v[190:191], v246, s[80:81]
	global_load_dwordx2 v[192:193], v246, s[80:81] offset:128
	s_add_u32 s80, s12, 0xe7400
	s_addc_u32 s81, s13, 0
	global_load_dwordx2 v[194:195], v246, s[80:81]
	global_load_dwordx2 v[196:197], v246, s[80:81] offset:128
	s_add_u32 s80, s12, 0x263400
	s_addc_u32 s81, s13, 0
	global_load_dwordx2 v[198:199], v246, s[80:81]
	global_load_dwordx2 v[200:201], v246, s[80:81] offset:128
	s_add_u32 s80, s12, 0x2af400
	s_addc_u32 s81, s13, 0
	global_load_dwordx2 v[202:203], v246, s[80:81]
	global_load_dwordx2 v[204:205], v246, s[80:81] offset:128
	s_add_u32 s80, s12, 0x2fb400
	s_addc_u32 s81, s13, 0
	global_load_dwordx2 v[206:207], v246, s[80:81]
	global_load_dwordx2 v[208:209], v246, s[80:81] offset:128
	s_add_u32 s80, s12, 0x347400
	s_addc_u32 s81, s13, 0
	global_load_dwordx2 v[210:211], v246, s[80:81]
	global_load_dwordx2 v[212:213], v246, s[80:81] offset:128
	s_cmp_lg_u32 s66, 0
	s_cbranch_scc1 .Lproj_epi_nogm
	s_add_u32 s80, s12, 0x2c00
	s_addc_u32 s81, s13, 0
	global_load_dwordx2 v[214:215], v246, s[80:81]
	global_load_dwordx2 v[216:217], v246, s[80:81] offset:128
	s_add_u32 s80, s12, 0x4ec00
	s_addc_u32 s81, s13, 0
	global_load_dwordx2 v[218:219], v246, s[80:81]
	global_load_dwordx2 v[220:221], v246, s[80:81] offset:128
	s_add_u32 s80, s12, 0x9ac00
	s_addc_u32 s81, s13, 0
	global_load_dwordx2 v[222:223], v246, s[80:81]
	global_load_dwordx2 v[224:225], v246, s[80:81] offset:128
	s_add_u32 s80, s12, 0xe6c00
	s_addc_u32 s81, s13, 0
	global_load_dwordx2 v[226:227], v246, s[80:81]
	global_load_dwordx2 v[228:229], v246, s[80:81] offset:128
	s_add_u32 s80, s12, 0x262c00
	s_addc_u32 s81, s13, 0
	global_load_dwordx2 v[230:231], v246, s[80:81]
	global_load_dwordx2 v[232:233], v246, s[80:81] offset:128
	s_add_u32 s80, s12, 0x2aec00
	s_addc_u32 s81, s13, 0
	global_load_dwordx2 v[234:235], v246, s[80:81]
	global_load_dwordx2 v[236:237], v246, s[80:81] offset:128
	s_add_u32 s80, s12, 0x2fac00
	s_addc_u32 s81, s13, 0
	global_load_dwordx2 v[238:239], v246, s[80:81]
	global_load_dwordx2 v[240:241], v246, s[80:81] offset:128
	s_add_u32 s80, s12, 0x346c00
	s_addc_u32 s81, s13, 0
	global_load_dwordx2 v[242:243], v246, s[80:81]
	global_load_dwordx2 v[244:245], v246, s[80:81] offset:128
.Lproj_epi_nogm:
	s_waitcnt vmcnt(0)
	v_mov_b32_e32 v156, v182
	v_mov_b32_e32 v157, v183
	v_ashrrev_i32_e32 v153, 31, v152
	v_lshlrev_b64 v[150:151], 12, v[152:153]
	s_cmp_lg_u32 s66, 0
	v_lshl_add_u64 v[168:169], s[14:15], 0, v[150:151]
	s_cselect_b64 s[30:31], -1, 0
	s_cmp_eq_u32 s66, 0
	s_nop 1
	v_cvt_f32_ubyte0_e32 v163, v156
	v_cvt_f32_ubyte1_e32 v164, v156
	v_cvt_f32_ubyte2_e32 v165, v156
	v_cvt_f32_ubyte3_e32 v166, v156
	v_cvt_f32_ubyte0_e32 v3, v157
	v_cvt_f32_ubyte1_e32 v150, v157
	v_cvt_f32_ubyte2_e32 v151, v157
	v_cvt_f32_ubyte3_e32 v153, v157
	v_lshl_add_u64 v[156:157], v[4:5], 1, v[168:169]
	s_cbranch_scc1 .LBB0_754
	v_mul_f32_e32 v168, 0x3b808081, v164
	v_mul_f32_e32 v169, 0x3b808081, v165
	v_mul_f32_e32 v170, 0x3b808081, v166
	v_mul_f32_e32 v171, 0x3b808081, v3
	v_mul_f32_e32 v167, 0x3b808081, v163
	v_mul_f32_e32 v168, v131, v168
	v_mul_f32_e32 v169, v132, v169
	v_mul_f32_e32 v170, v133, v170
	v_mul_f32_e32 v171, v126, v171
	v_mul_f32_e32 v172, 0x3b808081, v150
	v_mul_f32_e32 v173, 0x3b808081, v151
	v_mul_f32_e32 v174, 0x3b808081, v153
	v_mul_f32_e32 v167, v130, v167
	v_mul_f32_e32 v172, v127, v172
	v_mul_f32_e32 v173, v128, v173
	v_mul_f32_e32 v174, v129, v174
	v_cvt_pk_bf16_f32 v168, v167, v168
	v_cvt_pk_bf16_f32 v169, v169, v170
	v_cvt_pk_bf16_f32 v170, v171, v172
	v_cvt_pk_bf16_f32 v171, v173, v174
	global_store_dwordx4 v[156:157], v[168:171], off
	s_cbranch_execnz .LBB0_704
.LBB0_703:
	s_nop 0
	v_lshl_add_u64 v[168:169], v[154:155], 0, v[4:5]
	v_add_co_u32_e32 v168, vcc, 0x2000, v168
	v_rcp_f32_e32 v170, v163
	s_nop 0
	v_addc_co_u32_e32 v169, vcc, 0, v169, vcc
	v_mov_b32_e32 v168, v214
	v_mov_b32_e32 v169, v215
	v_rcp_f32_e32 v171, v164
	v_rcp_f32_e32 v164, v165
	v_rcp_f32_e32 v165, v166
	v_rcp_f32_e32 v166, v3
	v_rcp_f32_e32 v167, v150
	v_rcp_f32_e32 v150, v151
	v_rcp_f32_e32 v151, v153
	s_nop 1
	v_cvt_f32_ubyte3_e32 v173, v168
	v_cvt_f32_ubyte2_e32 v172, v168
	v_cvt_f32_ubyte1_e32 v175, v168
	v_cvt_f32_ubyte0_e32 v174, v168
	v_cvt_f32_ubyte3_e32 v177, v169
	v_cvt_f32_ubyte2_e32 v176, v169
	v_cvt_f32_ubyte1_e32 v179, v169
	v_cvt_f32_ubyte0_e32 v178, v169
	v_pk_mul_f32 v[168:169], v[170:171], v[174:175]
	v_pk_mul_f32 v[164:165], v[164:165], v[172:173]
	v_pk_mul_f32 v[166:167], v[166:167], v[178:179]
	v_pk_mul_f32 v[150:151], v[150:151], v[176:177]
	v_pk_mul_f32 v[132:133], v[132:133], v[164:165]
	v_pk_mul_f32 v[130:131], v[130:131], v[168:169]
	v_pk_mul_f32 v[128:129], v[128:129], v[150:151]
	v_pk_mul_f32 v[126:127], v[126:127], v[166:167]
.LBB0_704:
	v_or_b32_e32 v150, 0x80, v4
	v_ashrrev_i32_e32 v151, 31, v150
	v_lshl_add_u64 v[158:159], v[158:159], 0, v[150:151]
	v_mov_b32_e32 v158, v184
	v_mov_b32_e32 v159, v185
	v_cndmask_b32_e64 v3, 0, 1, s[30:31]
	v_cmp_ne_u32_e64 s[6:7], 1, v3
	s_andn2_b64 vcc, exec, s[30:31]
	s_nop 1
	v_cvt_f32_ubyte0_e32 v163, v158
	v_cvt_f32_ubyte1_e32 v164, v158
	v_cvt_f32_ubyte2_e32 v165, v158
	v_cvt_f32_ubyte3_e32 v166, v158
	v_cvt_f32_ubyte0_e32 v3, v159
	v_cvt_f32_ubyte1_e32 v153, v159
	v_cvt_f32_ubyte2_e32 v158, v159
	v_cvt_f32_ubyte3_e32 v159, v159
	s_cbranch_vccnz .LBB0_755
	v_mul_f32_e32 v168, 0x3b808081, v164
	v_mul_f32_e32 v169, 0x3b808081, v165
	v_mul_f32_e32 v170, 0x3b808081, v166
	v_mul_f32_e32 v171, 0x3b808081, v3
	v_mul_f32_e32 v167, 0x3b808081, v163
	v_mul_f32_e32 v168, v99, v168
	v_mul_f32_e32 v169, v100, v169
	v_mul_f32_e32 v170, v101, v170
	v_mul_f32_e32 v171, v94, v171
	v_mul_f32_e32 v172, 0x3b808081, v153
	v_mul_f32_e32 v173, 0x3b808081, v158
	v_mul_f32_e32 v174, 0x3b808081, v159
	v_mul_f32_e32 v167, v98, v167
	v_mul_f32_e32 v172, v95, v172
	v_mul_f32_e32 v173, v96, v173
	v_mul_f32_e32 v174, v97, v174
	v_cvt_pk_bf16_f32 v168, v167, v168
	v_cvt_pk_bf16_f32 v169, v169, v170
	v_cvt_pk_bf16_f32 v170, v171, v172
	v_cvt_pk_bf16_f32 v171, v173, v174
	global_store_dwordx4 v[156:157], v[168:171], off offset:256
	s_cbranch_execnz .LBB0_707
.LBB0_706:
	v_lshl_add_u64 v[154:155], v[154:155], 0, v[150:151]
	v_add_co_u32_e32 v154, vcc, 0x2000, v154
	v_rcp_f32_e32 v156, v163
	s_nop 0
	v_addc_co_u32_e32 v155, vcc, 0, v155, vcc
	v_mov_b32_e32 v154, v216
	v_mov_b32_e32 v155, v217
	v_rcp_f32_e32 v157, v164
	v_rcp_f32_e32 v164, v165
	v_rcp_f32_e32 v165, v166
	v_rcp_f32_e32 v166, v3
	v_rcp_f32_e32 v167, v153
	v_rcp_f32_e32 v158, v158
	v_rcp_f32_e32 v159, v159
	s_nop 1
	v_cvt_f32_ubyte3_e32 v169, v154
	v_cvt_f32_ubyte2_e32 v168, v154
	v_cvt_f32_ubyte1_e32 v171, v154
	v_cvt_f32_ubyte0_e32 v170, v154
	v_cvt_f32_ubyte3_e32 v173, v155
	v_cvt_f32_ubyte2_e32 v172, v155
	v_cvt_f32_ubyte1_e32 v175, v155
	v_cvt_f32_ubyte0_e32 v174, v155
	v_pk_mul_f32 v[154:155], v[156:157], v[170:171]
	v_pk_mul_f32 v[156:157], v[164:165], v[168:169]
	v_pk_mul_f32 v[164:165], v[166:167], v[174:175]
	v_pk_mul_f32 v[158:159], v[158:159], v[172:173]
	v_pk_mul_f32 v[100:101], v[100:101], v[156:157]
	v_pk_mul_f32 v[98:99], v[98:99], v[154:155]
	v_pk_mul_f32 v[96:97], v[96:97], v[158:159]
	v_pk_mul_f32 v[94:95], v[94:95], v[164:165]
.LBB0_707:
	v_or_b32_e32 v156, 16, v152
	v_mov_b64_e32 v[154:155], s[12:13]
	v_mad_i64_i32 v[154:155], s[30:31], v156, s63, v[154:155]
	v_lshl_add_u64 v[158:159], v[154:155], 0, s[20:21]
	v_lshl_add_u64 v[164:165], v[158:159], 0, v[4:5]
	v_mov_b32_e32 v168, v186
	v_mov_b32_e32 v169, v187
	v_ashrrev_i32_e32 v157, 31, v156
	v_lshlrev_b64 v[156:157], 12, v[156:157]
	v_lshl_add_u64 v[156:157], s[14:15], 0, v[156:157]
	s_and_b64 vcc, exec, s[6:7]
	v_lshl_add_u64 v[156:157], v[4:5], 1, v[156:157]
	s_nop 1
	v_cvt_f32_ubyte0_e32 v165, v168
	v_cvt_f32_ubyte1_e32 v166, v168
	v_cvt_f32_ubyte2_e32 v167, v168
	v_cvt_f32_ubyte3_e32 v168, v168
	v_cvt_f32_ubyte0_e32 v3, v169
	v_cvt_f32_ubyte1_e32 v153, v169
	v_cvt_f32_ubyte2_e32 v163, v169
	v_cvt_f32_ubyte3_e32 v164, v169
	s_cbranch_vccnz .LBB0_756
	v_mul_f32_e32 v170, 0x3b808081, v166
	v_mul_f32_e32 v171, 0x3b808081, v167
	v_mul_f32_e32 v172, 0x3b808081, v168
	v_mul_f32_e32 v173, 0x3b808081, v3
	v_mul_f32_e32 v169, 0x3b808081, v165
	v_mul_f32_e32 v170, v123, v170
	v_mul_f32_e32 v171, v124, v171
	v_mul_f32_e32 v172, v125, v172
	v_mul_f32_e32 v173, v118, v173
	v_mul_f32_e32 v174, 0x3b808081, v153
	v_mul_f32_e32 v175, 0x3b808081, v163
	v_mul_f32_e32 v176, 0x3b808081, v164
	v_mul_f32_e32 v169, v122, v169
	v_mul_f32_e32 v174, v119, v174
	v_mul_f32_e32 v175, v120, v175
	v_mul_f32_e32 v176, v121, v176
	v_cvt_pk_bf16_f32 v170, v169, v170
	v_cvt_pk_bf16_f32 v171, v171, v172
	v_cvt_pk_bf16_f32 v172, v173, v174
	v_cvt_pk_bf16_f32 v173, v175, v176
	global_store_dwordx4 v[156:157], v[170:173], off
	s_cbranch_execnz .LBB0_710
.LBB0_709:
	s_nop 0
	v_lshl_add_u64 v[170:171], v[154:155], 0, v[4:5]
	v_add_co_u32_e32 v170, vcc, 0x2000, v170
	v_rcp_f32_e32 v172, v165
	s_nop 0
	v_addc_co_u32_e32 v171, vcc, 0, v171, vcc
	v_mov_b32_e32 v170, v218
	v_mov_b32_e32 v171, v219
	v_rcp_f32_e32 v173, v166
	v_rcp_f32_e32 v166, v167
	v_rcp_f32_e32 v167, v168
	v_rcp_f32_e32 v168, v3
	v_rcp_f32_e32 v169, v153
	v_rcp_f32_e32 v174, v163
	v_rcp_f32_e32 v175, v164
	s_nop 1
	v_cvt_f32_ubyte3_e32 v165, v170
	v_cvt_f32_ubyte2_e32 v164, v170
	v_cvt_f32_ubyte1_e32 v177, v170
	v_cvt_f32_ubyte0_e32 v176, v170
	v_cvt_f32_ubyte3_e32 v179, v171
	v_cvt_f32_ubyte2_e32 v178, v171
	v_cvt_f32_ubyte1_e32 v181, v171
	v_cvt_f32_ubyte0_e32 v180, v171
	v_pk_mul_f32 v[170:171], v[172:173], v[176:177]
	v_pk_mul_f32 v[164:165], v[166:167], v[164:165]
	v_pk_mul_f32 v[166:167], v[168:169], v[180:181]
	v_pk_mul_f32 v[168:169], v[174:175], v[178:179]
	v_pk_mul_f32 v[124:125], v[124:125], v[164:165]
	v_pk_mul_f32 v[122:123], v[122:123], v[170:171]
	v_pk_mul_f32 v[120:121], v[120:121], v[168:169]
	v_pk_mul_f32 v[118:119], v[118:119], v[166:167]
.LBB0_710:
	v_lshl_add_u64 v[158:159], v[158:159], 0, v[150:151]
	v_mov_b32_e32 v158, v188
	v_mov_b32_e32 v159, v189
	s_and_b64 vcc, exec, s[6:7]
	s_nop 1
	v_cvt_f32_ubyte0_e32 v163, v158
	v_cvt_f32_ubyte1_e32 v164, v158
	v_cvt_f32_ubyte2_e32 v165, v158
	v_cvt_f32_ubyte3_e32 v166, v158
	v_cvt_f32_ubyte0_e32 v3, v159
	v_cvt_f32_ubyte1_e32 v153, v159
	v_cvt_f32_ubyte2_e32 v158, v159
	v_cvt_f32_ubyte3_e32 v159, v159
	s_cbranch_vccnz .LBB0_757
	v_mul_f32_e32 v168, 0x3b808081, v164
	v_mul_f32_e32 v169, 0x3b808081, v165
	v_mul_f32_e32 v170, 0x3b808081, v166
	v_mul_f32_e32 v171, 0x3b808081, v3
	v_mul_f32_e32 v167, 0x3b808081, v163
	v_mul_f32_e32 v168, v91, v168
	v_mul_f32_e32 v169, v92, v169
	v_mul_f32_e32 v170, v93, v170
	v_mul_f32_e32 v171, v86, v171
	v_mul_f32_e32 v172, 0x3b808081, v153
	v_mul_f32_e32 v173, 0x3b808081, v158
	v_mul_f32_e32 v174, 0x3b808081, v159
	v_mul_f32_e32 v167, v90, v167
	v_mul_f32_e32 v172, v87, v172
	v_mul_f32_e32 v173, v88, v173
	v_mul_f32_e32 v174, v89, v174
	v_cvt_pk_bf16_f32 v168, v167, v168
	v_cvt_pk_bf16_f32 v169, v169, v170
	v_cvt_pk_bf16_f32 v170, v171, v172
	v_cvt_pk_bf16_f32 v171, v173, v174
	global_store_dwordx4 v[156:157], v[168:171], off offset:256
	s_cbranch_execnz .LBB0_713
.LBB0_712:
	v_lshl_add_u64 v[154:155], v[154:155], 0, v[150:151]
	v_add_co_u32_e32 v154, vcc, 0x2000, v154
	v_rcp_f32_e32 v156, v163
	s_nop 0
	v_addc_co_u32_e32 v155, vcc, 0, v155, vcc
	v_mov_b32_e32 v154, v220
	v_mov_b32_e32 v155, v221
	v_rcp_f32_e32 v157, v164
	v_rcp_f32_e32 v164, v165
	v_rcp_f32_e32 v165, v166
	v_rcp_f32_e32 v166, v3
	v_rcp_f32_e32 v167, v153
	v_rcp_f32_e32 v158, v158
	v_rcp_f32_e32 v159, v159
	s_nop 1
	v_cvt_f32_ubyte3_e32 v169, v154
	v_cvt_f32_ubyte2_e32 v168, v154
	v_cvt_f32_ubyte1_e32 v171, v154
	v_cvt_f32_ubyte0_e32 v170, v154
	v_cvt_f32_ubyte3_e32 v173, v155
	v_cvt_f32_ubyte2_e32 v172, v155
	v_cvt_f32_ubyte1_e32 v175, v155
	v_cvt_f32_ubyte0_e32 v174, v155
	v_pk_mul_f32 v[154:155], v[156:157], v[170:171]
	v_pk_mul_f32 v[156:157], v[164:165], v[168:169]
	v_pk_mul_f32 v[164:165], v[166:167], v[174:175]
	v_pk_mul_f32 v[158:159], v[158:159], v[172:173]
	v_pk_mul_f32 v[92:93], v[92:93], v[156:157]
	v_pk_mul_f32 v[90:91], v[90:91], v[154:155]
	v_pk_mul_f32 v[88:89], v[88:89], v[158:159]
	v_pk_mul_f32 v[86:87], v[86:87], v[164:165]
.LBB0_713:
	v_or_b32_e32 v156, 32, v152
	v_mov_b64_e32 v[154:155], s[12:13]
	v_mad_i64_i32 v[154:155], s[30:31], v156, s63, v[154:155]
	v_lshl_add_u64 v[158:159], v[154:155], 0, s[20:21]
	v_lshl_add_u64 v[164:165], v[158:159], 0, v[4:5]
	v_mov_b32_e32 v168, v190
	v_mov_b32_e32 v169, v191
	v_ashrrev_i32_e32 v157, 31, v156
	v_lshlrev_b64 v[156:157], 12, v[156:157]
	v_lshl_add_u64 v[156:157], s[14:15], 0, v[156:157]
	s_and_b64 vcc, exec, s[6:7]
	v_lshl_add_u64 v[156:157], v[4:5], 1, v[156:157]
	s_nop 1
	v_cvt_f32_ubyte0_e32 v165, v168
	v_cvt_f32_ubyte1_e32 v166, v168
	v_cvt_f32_ubyte2_e32 v167, v168
	v_cvt_f32_ubyte3_e32 v168, v168
	v_cvt_f32_ubyte0_e32 v3, v169
	v_cvt_f32_ubyte1_e32 v153, v169
	v_cvt_f32_ubyte2_e32 v163, v169
	v_cvt_f32_ubyte3_e32 v164, v169
	s_cbranch_vccnz .LBB0_758
	v_mul_f32_e32 v170, 0x3b808081, v166
	v_mul_f32_e32 v171, 0x3b808081, v167
	v_mul_f32_e32 v172, 0x3b808081, v168
	v_mul_f32_e32 v173, 0x3b808081, v3
	v_mul_f32_e32 v169, 0x3b808081, v165
	v_mul_f32_e32 v170, v115, v170
	v_mul_f32_e32 v171, v116, v171
	v_mul_f32_e32 v172, v117, v172
	v_mul_f32_e32 v173, v110, v173
	v_mul_f32_e32 v174, 0x3b808081, v153
	v_mul_f32_e32 v175, 0x3b808081, v163
	v_mul_f32_e32 v176, 0x3b808081, v164
	v_mul_f32_e32 v169, v114, v169
	v_mul_f32_e32 v174, v111, v174
	v_mul_f32_e32 v175, v112, v175
	v_mul_f32_e32 v176, v113, v176
	v_cvt_pk_bf16_f32 v170, v169, v170
	v_cvt_pk_bf16_f32 v171, v171, v172
	v_cvt_pk_bf16_f32 v172, v173, v174
	v_cvt_pk_bf16_f32 v173, v175, v176
	global_store_dwordx4 v[156:157], v[170:173], off
	s_cbranch_execnz .LBB0_716
.LBB0_715:
	s_nop 0
	v_lshl_add_u64 v[170:171], v[154:155], 0, v[4:5]
	v_add_co_u32_e32 v170, vcc, 0x2000, v170
	v_rcp_f32_e32 v172, v165
	s_nop 0
	v_addc_co_u32_e32 v171, vcc, 0, v171, vcc
	v_mov_b32_e32 v170, v222
	v_mov_b32_e32 v171, v223
	v_rcp_f32_e32 v173, v166
	v_rcp_f32_e32 v166, v167
	v_rcp_f32_e32 v167, v168
	v_rcp_f32_e32 v168, v3
	v_rcp_f32_e32 v169, v153
	v_rcp_f32_e32 v174, v163
	v_rcp_f32_e32 v175, v164
	s_nop 1
	v_cvt_f32_ubyte3_e32 v165, v170
	v_cvt_f32_ubyte2_e32 v164, v170
	v_cvt_f32_ubyte1_e32 v177, v170
	v_cvt_f32_ubyte0_e32 v176, v170
	v_cvt_f32_ubyte3_e32 v179, v171
	v_cvt_f32_ubyte2_e32 v178, v171
	v_cvt_f32_ubyte1_e32 v181, v171
	v_cvt_f32_ubyte0_e32 v180, v171
	v_pk_mul_f32 v[170:171], v[172:173], v[176:177]
	v_pk_mul_f32 v[164:165], v[166:167], v[164:165]
	v_pk_mul_f32 v[166:167], v[168:169], v[180:181]
	v_pk_mul_f32 v[168:169], v[174:175], v[178:179]
	v_pk_mul_f32 v[116:117], v[116:117], v[164:165]
	v_pk_mul_f32 v[114:115], v[114:115], v[170:171]
	v_pk_mul_f32 v[112:113], v[112:113], v[168:169]
	v_pk_mul_f32 v[110:111], v[110:111], v[166:167]
.LBB0_716:
	v_lshl_add_u64 v[158:159], v[158:159], 0, v[150:151]
	v_mov_b32_e32 v158, v192
	v_mov_b32_e32 v159, v193
	s_and_b64 vcc, exec, s[6:7]
	s_nop 1
	v_cvt_f32_ubyte0_e32 v163, v158
	v_cvt_f32_ubyte1_e32 v164, v158
	v_cvt_f32_ubyte2_e32 v165, v158
	v_cvt_f32_ubyte3_e32 v166, v158
	v_cvt_f32_ubyte0_e32 v3, v159
	v_cvt_f32_ubyte1_e32 v153, v159
	v_cvt_f32_ubyte2_e32 v158, v159
	v_cvt_f32_ubyte3_e32 v159, v159
	s_cbranch_vccnz .LBB0_759
	v_mul_f32_e32 v168, 0x3b808081, v164
	v_mul_f32_e32 v169, 0x3b808081, v165
	v_mul_f32_e32 v170, 0x3b808081, v166
	v_mul_f32_e32 v171, 0x3b808081, v3
	v_mul_f32_e32 v167, 0x3b808081, v163
	v_mul_f32_e32 v168, v83, v168
	v_mul_f32_e32 v169, v84, v169
	v_mul_f32_e32 v170, v85, v170
	v_mul_f32_e32 v171, v78, v171
	v_mul_f32_e32 v172, 0x3b808081, v153
	v_mul_f32_e32 v173, 0x3b808081, v158
	v_mul_f32_e32 v174, 0x3b808081, v159
	v_mul_f32_e32 v167, v82, v167
	v_mul_f32_e32 v172, v79, v172
	v_mul_f32_e32 v173, v80, v173
	v_mul_f32_e32 v174, v81, v174
	v_cvt_pk_bf16_f32 v168, v167, v168
	v_cvt_pk_bf16_f32 v169, v169, v170
	v_cvt_pk_bf16_f32 v170, v171, v172
	v_cvt_pk_bf16_f32 v171, v173, v174
	global_store_dwordx4 v[156:157], v[168:171], off offset:256
	s_cbranch_execnz .LBB0_719
.LBB0_718:
	v_lshl_add_u64 v[154:155], v[154:155], 0, v[150:151]
	v_add_co_u32_e32 v154, vcc, 0x2000, v154
	v_rcp_f32_e32 v156, v163
	s_nop 0
	v_addc_co_u32_e32 v155, vcc, 0, v155, vcc
	v_mov_b32_e32 v154, v224
	v_mov_b32_e32 v155, v225
	v_rcp_f32_e32 v157, v164
	v_rcp_f32_e32 v164, v165
	v_rcp_f32_e32 v165, v166
	v_rcp_f32_e32 v166, v3
	v_rcp_f32_e32 v167, v153
	v_rcp_f32_e32 v158, v158
	v_rcp_f32_e32 v159, v159
	s_nop 1
	v_cvt_f32_ubyte3_e32 v169, v154
	v_cvt_f32_ubyte2_e32 v168, v154
	v_cvt_f32_ubyte1_e32 v171, v154
	v_cvt_f32_ubyte0_e32 v170, v154
	v_cvt_f32_ubyte3_e32 v173, v155
	v_cvt_f32_ubyte2_e32 v172, v155
	v_cvt_f32_ubyte1_e32 v175, v155
	v_cvt_f32_ubyte0_e32 v174, v155
	v_pk_mul_f32 v[154:155], v[156:157], v[170:171]
	v_pk_mul_f32 v[156:157], v[164:165], v[168:169]
	v_pk_mul_f32 v[164:165], v[166:167], v[174:175]
	v_pk_mul_f32 v[158:159], v[158:159], v[172:173]
	v_pk_mul_f32 v[84:85], v[84:85], v[156:157]
	v_pk_mul_f32 v[82:83], v[82:83], v[154:155]
	v_pk_mul_f32 v[80:81], v[80:81], v[158:159]
	v_pk_mul_f32 v[78:79], v[78:79], v[164:165]
.LBB0_719:
	v_or_b32_e32 v156, 48, v152
	v_mov_b64_e32 v[154:155], s[12:13]
	v_mad_i64_i32 v[154:155], s[30:31], v156, s63, v[154:155]
	v_lshl_add_u64 v[158:159], v[154:155], 0, s[20:21]
	v_lshl_add_u64 v[164:165], v[158:159], 0, v[4:5]
	v_mov_b32_e32 v168, v194
	v_mov_b32_e32 v169, v195
	v_ashrrev_i32_e32 v157, 31, v156
	v_lshlrev_b64 v[156:157], 12, v[156:157]
	v_lshl_add_u64 v[156:157], s[14:15], 0, v[156:157]
	s_and_b64 vcc, exec, s[6:7]
	v_lshl_add_u64 v[156:157], v[4:5], 1, v[156:157]
	s_nop 1
	v_cvt_f32_ubyte0_e32 v165, v168
	v_cvt_f32_ubyte1_e32 v166, v168
	v_cvt_f32_ubyte2_e32 v167, v168
	v_cvt_f32_ubyte3_e32 v168, v168
	v_cvt_f32_ubyte0_e32 v3, v169
	v_cvt_f32_ubyte1_e32 v153, v169
	v_cvt_f32_ubyte2_e32 v163, v169
	v_cvt_f32_ubyte3_e32 v164, v169
	s_cbranch_vccnz .LBB0_760
	v_mul_f32_e32 v170, 0x3b808081, v166
	v_mul_f32_e32 v171, 0x3b808081, v167
	v_mul_f32_e32 v172, 0x3b808081, v168
	v_mul_f32_e32 v173, 0x3b808081, v3
	v_mul_f32_e32 v169, 0x3b808081, v165
	v_mul_f32_e32 v170, v107, v170
	v_mul_f32_e32 v171, v108, v171
	v_mul_f32_e32 v172, v109, v172
	v_mul_f32_e32 v173, v102, v173
	v_mul_f32_e32 v174, 0x3b808081, v153
	v_mul_f32_e32 v175, 0x3b808081, v163
	v_mul_f32_e32 v176, 0x3b808081, v164
	v_mul_f32_e32 v169, v106, v169
	v_mul_f32_e32 v174, v103, v174
	v_mul_f32_e32 v175, v104, v175
	v_mul_f32_e32 v176, v105, v176
	v_cvt_pk_bf16_f32 v170, v169, v170
	v_cvt_pk_bf16_f32 v171, v171, v172
	v_cvt_pk_bf16_f32 v172, v173, v174
	v_cvt_pk_bf16_f32 v173, v175, v176
	global_store_dwordx4 v[156:157], v[170:173], off
	s_cbranch_execnz .LBB0_722
.LBB0_721:
	s_nop 0
	v_lshl_add_u64 v[170:171], v[154:155], 0, v[4:5]
	v_add_co_u32_e32 v170, vcc, 0x2000, v170
	v_rcp_f32_e32 v172, v165
	s_nop 0
	v_addc_co_u32_e32 v171, vcc, 0, v171, vcc
	v_mov_b32_e32 v170, v226
	v_mov_b32_e32 v171, v227
	v_rcp_f32_e32 v173, v166
	v_rcp_f32_e32 v166, v167
	v_rcp_f32_e32 v167, v168
	v_rcp_f32_e32 v168, v3
	v_rcp_f32_e32 v169, v153
	v_rcp_f32_e32 v174, v163
	v_rcp_f32_e32 v175, v164
	s_nop 1
	v_cvt_f32_ubyte3_e32 v165, v170
	v_cvt_f32_ubyte2_e32 v164, v170
	v_cvt_f32_ubyte1_e32 v177, v170
	v_cvt_f32_ubyte0_e32 v176, v170
	v_cvt_f32_ubyte3_e32 v179, v171
	v_cvt_f32_ubyte2_e32 v178, v171
	v_cvt_f32_ubyte1_e32 v181, v171
	v_cvt_f32_ubyte0_e32 v180, v171
	v_pk_mul_f32 v[170:171], v[172:173], v[176:177]
	v_pk_mul_f32 v[164:165], v[166:167], v[164:165]
	v_pk_mul_f32 v[166:167], v[168:169], v[180:181]
	v_pk_mul_f32 v[168:169], v[174:175], v[178:179]
	v_pk_mul_f32 v[108:109], v[108:109], v[164:165]
	v_pk_mul_f32 v[106:107], v[106:107], v[170:171]
	v_pk_mul_f32 v[104:105], v[104:105], v[168:169]
	v_pk_mul_f32 v[102:103], v[102:103], v[166:167]
.LBB0_722:
	v_lshl_add_u64 v[158:159], v[158:159], 0, v[150:151]
	v_mov_b32_e32 v158, v196
	v_mov_b32_e32 v159, v197
	s_and_b64 vcc, exec, s[6:7]
	s_nop 1
	v_cvt_f32_ubyte0_e32 v163, v158
	v_cvt_f32_ubyte1_e32 v164, v158
	v_cvt_f32_ubyte2_e32 v165, v158
	v_cvt_f32_ubyte3_e32 v166, v158
	v_cvt_f32_ubyte0_e32 v3, v159
	v_cvt_f32_ubyte1_e32 v153, v159
	v_cvt_f32_ubyte2_e32 v158, v159
	v_cvt_f32_ubyte3_e32 v159, v159
	s_cbranch_vccnz .LBB0_761
	v_mul_f32_e32 v168, 0x3b808081, v164
	v_mul_f32_e32 v169, 0x3b808081, v165
	v_mul_f32_e32 v170, 0x3b808081, v166
	v_mul_f32_e32 v171, 0x3b808081, v3
	v_mul_f32_e32 v167, 0x3b808081, v163
	v_mul_f32_e32 v168, v75, v168
	v_mul_f32_e32 v169, v76, v169
	v_mul_f32_e32 v170, v77, v170
	v_mul_f32_e32 v171, v70, v171
	v_mul_f32_e32 v172, 0x3b808081, v153
	v_mul_f32_e32 v173, 0x3b808081, v158
	v_mul_f32_e32 v174, 0x3b808081, v159
	v_mul_f32_e32 v167, v74, v167
	v_mul_f32_e32 v172, v71, v172
	v_mul_f32_e32 v173, v72, v173
	v_mul_f32_e32 v174, v73, v174
	v_cvt_pk_bf16_f32 v168, v167, v168
	v_cvt_pk_bf16_f32 v169, v169, v170
	v_cvt_pk_bf16_f32 v170, v171, v172
	v_cvt_pk_bf16_f32 v171, v173, v174
	global_store_dwordx4 v[156:157], v[168:171], off offset:256
	s_cbranch_execnz .LBB0_725
.LBB0_724:
	v_lshl_add_u64 v[154:155], v[154:155], 0, v[150:151]
	v_add_co_u32_e32 v154, vcc, 0x2000, v154
	v_rcp_f32_e32 v156, v163
	s_nop 0
	v_addc_co_u32_e32 v155, vcc, 0, v155, vcc
	v_mov_b32_e32 v154, v228
	v_mov_b32_e32 v155, v229
	v_rcp_f32_e32 v157, v164
	v_rcp_f32_e32 v164, v165
	v_rcp_f32_e32 v165, v166
	v_rcp_f32_e32 v166, v3
	v_rcp_f32_e32 v167, v153
	v_rcp_f32_e32 v158, v158
	v_rcp_f32_e32 v159, v159
	s_nop 1
	v_cvt_f32_ubyte3_e32 v169, v154
	v_cvt_f32_ubyte2_e32 v168, v154
	v_cvt_f32_ubyte1_e32 v171, v154
	v_cvt_f32_ubyte0_e32 v170, v154
	v_cvt_f32_ubyte3_e32 v173, v155
	v_cvt_f32_ubyte2_e32 v172, v155
	v_cvt_f32_ubyte1_e32 v175, v155
	v_cvt_f32_ubyte0_e32 v174, v155
	v_pk_mul_f32 v[154:155], v[156:157], v[170:171]
	v_pk_mul_f32 v[156:157], v[164:165], v[168:169]
	v_pk_mul_f32 v[164:165], v[166:167], v[174:175]
	v_pk_mul_f32 v[158:159], v[158:159], v[172:173]
	v_pk_mul_f32 v[76:77], v[76:77], v[156:157]
	v_pk_mul_f32 v[74:75], v[74:75], v[154:155]
	v_pk_mul_f32 v[72:73], v[72:73], v[158:159]
	v_pk_mul_f32 v[70:71], v[70:71], v[164:165]
.LBB0_725:
	v_add_u32_e32 v156, 0x80, v152
	v_mov_b64_e32 v[154:155], s[12:13]
	v_mad_i64_i32 v[154:155], s[30:31], v156, s63, v[154:155]
	v_lshl_add_u64 v[158:159], v[154:155], 0, s[20:21]
	v_lshl_add_u64 v[164:165], v[158:159], 0, v[4:5]
	v_mov_b32_e32 v168, v198
	v_mov_b32_e32 v169, v199
	v_ashrrev_i32_e32 v157, 31, v156
	v_lshlrev_b64 v[156:157], 12, v[156:157]
	v_lshl_add_u64 v[156:157], s[14:15], 0, v[156:157]
	s_and_b64 vcc, exec, s[6:7]
	v_lshl_add_u64 v[156:157], v[4:5], 1, v[156:157]
	s_nop 1
	v_cvt_f32_ubyte0_e32 v165, v168
	v_cvt_f32_ubyte1_e32 v166, v168
	v_cvt_f32_ubyte2_e32 v167, v168
	v_cvt_f32_ubyte3_e32 v168, v168
	v_cvt_f32_ubyte0_e32 v3, v169
	v_cvt_f32_ubyte1_e32 v153, v169
	v_cvt_f32_ubyte2_e32 v163, v169
	v_cvt_f32_ubyte3_e32 v164, v169
	s_cbranch_vccnz .LBB0_762
	v_mul_f32_e32 v170, 0x3b808081, v166
	v_mul_f32_e32 v171, 0x3b808081, v167
	v_mul_f32_e32 v172, 0x3b808081, v168
	v_mul_f32_e32 v173, 0x3b808081, v3
	v_mul_f32_e32 v169, 0x3b808081, v165
	v_mul_f32_e32 v170, v67, v170
	v_mul_f32_e32 v171, v68, v171
	v_mul_f32_e32 v172, v69, v172
	v_mul_f32_e32 v173, v62, v173
	v_mul_f32_e32 v174, 0x3b808081, v153
	v_mul_f32_e32 v175, 0x3b808081, v163
	v_mul_f32_e32 v176, 0x3b808081, v164
	v_mul_f32_e32 v169, v66, v169
	v_mul_f32_e32 v174, v63, v174
	v_mul_f32_e32 v175, v64, v175
	v_mul_f32_e32 v176, v65, v176
	v_cvt_pk_bf16_f32 v170, v169, v170
	v_cvt_pk_bf16_f32 v171, v171, v172
	v_cvt_pk_bf16_f32 v172, v173, v174
	v_cvt_pk_bf16_f32 v173, v175, v176
	global_store_dwordx4 v[156:157], v[170:173], off
	s_cbranch_execnz .LBB0_728
.LBB0_727:
	s_nop 0
	v_lshl_add_u64 v[170:171], v[154:155], 0, v[4:5]
	v_add_co_u32_e32 v170, vcc, 0x2000, v170
	v_rcp_f32_e32 v172, v165
	s_nop 0
	v_addc_co_u32_e32 v171, vcc, 0, v171, vcc
	v_mov_b32_e32 v170, v230
	v_mov_b32_e32 v171, v231
	v_rcp_f32_e32 v173, v166
	v_rcp_f32_e32 v166, v167
	v_rcp_f32_e32 v167, v168
	v_rcp_f32_e32 v168, v3
	v_rcp_f32_e32 v169, v153
	v_rcp_f32_e32 v174, v163
	v_rcp_f32_e32 v175, v164
	s_nop 1
	v_cvt_f32_ubyte3_e32 v165, v170
	v_cvt_f32_ubyte2_e32 v164, v170
	v_cvt_f32_ubyte1_e32 v177, v170
	v_cvt_f32_ubyte0_e32 v176, v170
	v_cvt_f32_ubyte3_e32 v179, v171
	v_cvt_f32_ubyte2_e32 v178, v171
	v_cvt_f32_ubyte1_e32 v181, v171
	v_cvt_f32_ubyte0_e32 v180, v171
	v_pk_mul_f32 v[170:171], v[172:173], v[176:177]
	v_pk_mul_f32 v[164:165], v[166:167], v[164:165]
	v_pk_mul_f32 v[166:167], v[168:169], v[180:181]
	v_pk_mul_f32 v[168:169], v[174:175], v[178:179]
	v_pk_mul_f32 v[68:69], v[68:69], v[164:165]
	v_pk_mul_f32 v[66:67], v[66:67], v[170:171]
	v_pk_mul_f32 v[64:65], v[64:65], v[168:169]
	v_pk_mul_f32 v[62:63], v[62:63], v[166:167]
.LBB0_728:
	v_lshl_add_u64 v[158:159], v[158:159], 0, v[150:151]
	v_mov_b32_e32 v158, v200
	v_mov_b32_e32 v159, v201
	s_and_b64 vcc, exec, s[6:7]
	s_nop 1
	v_cvt_f32_ubyte0_e32 v163, v158
	v_cvt_f32_ubyte1_e32 v164, v158
	v_cvt_f32_ubyte2_e32 v165, v158
	v_cvt_f32_ubyte3_e32 v166, v158
	v_cvt_f32_ubyte0_e32 v3, v159
	v_cvt_f32_ubyte1_e32 v153, v159
	v_cvt_f32_ubyte2_e32 v158, v159
	v_cvt_f32_ubyte3_e32 v159, v159
	s_cbranch_vccnz .LBB0_763
	v_mul_f32_e32 v168, 0x3b808081, v164
	v_mul_f32_e32 v169, 0x3b808081, v165
	v_mul_f32_e32 v170, 0x3b808081, v166
	v_mul_f32_e32 v171, 0x3b808081, v3
	v_mul_f32_e32 v167, 0x3b808081, v163
	v_mul_f32_e32 v168, v35, v168
	v_mul_f32_e32 v169, v36, v169
	v_mul_f32_e32 v170, v37, v170
	v_mul_f32_e32 v171, v30, v171
	v_mul_f32_e32 v172, 0x3b808081, v153
	v_mul_f32_e32 v173, 0x3b808081, v158
	v_mul_f32_e32 v174, 0x3b808081, v159
	v_mul_f32_e32 v167, v34, v167
	v_mul_f32_e32 v172, v31, v172
	v_mul_f32_e32 v173, v32, v173
	v_mul_f32_e32 v174, v33, v174
	v_cvt_pk_bf16_f32 v168, v167, v168
	v_cvt_pk_bf16_f32 v169, v169, v170
	v_cvt_pk_bf16_f32 v170, v171, v172
	v_cvt_pk_bf16_f32 v171, v173, v174
	global_store_dwordx4 v[156:157], v[168:171], off offset:256
	s_cbranch_execnz .LBB0_731
.LBB0_730:
	v_lshl_add_u64 v[154:155], v[154:155], 0, v[150:151]
	v_add_co_u32_e32 v154, vcc, 0x2000, v154
	v_rcp_f32_e32 v156, v163
	s_nop 0
	v_addc_co_u32_e32 v155, vcc, 0, v155, vcc
	v_mov_b32_e32 v154, v232
	v_mov_b32_e32 v155, v233
	v_rcp_f32_e32 v157, v164
	v_rcp_f32_e32 v164, v165
	v_rcp_f32_e32 v165, v166
	v_rcp_f32_e32 v166, v3
	v_rcp_f32_e32 v167, v153
	v_rcp_f32_e32 v158, v158
	v_rcp_f32_e32 v159, v159
	s_nop 1
	v_cvt_f32_ubyte3_e32 v169, v154
	v_cvt_f32_ubyte2_e32 v168, v154
	v_cvt_f32_ubyte1_e32 v171, v154
	v_cvt_f32_ubyte0_e32 v170, v154
	v_cvt_f32_ubyte3_e32 v173, v155
	v_cvt_f32_ubyte2_e32 v172, v155
	v_cvt_f32_ubyte1_e32 v175, v155
	v_cvt_f32_ubyte0_e32 v174, v155
	v_pk_mul_f32 v[154:155], v[156:157], v[170:171]
	v_pk_mul_f32 v[156:157], v[164:165], v[168:169]
	v_pk_mul_f32 v[164:165], v[166:167], v[174:175]
	v_pk_mul_f32 v[158:159], v[158:159], v[172:173]
	v_pk_mul_f32 v[36:37], v[36:37], v[156:157]
	v_pk_mul_f32 v[34:35], v[34:35], v[154:155]
	v_pk_mul_f32 v[32:33], v[32:33], v[158:159]
	v_pk_mul_f32 v[30:31], v[30:31], v[164:165]
.LBB0_731:
	v_add_u32_e32 v156, 0x90, v152
	v_mov_b64_e32 v[154:155], s[12:13]
	v_mad_i64_i32 v[154:155], s[30:31], v156, s63, v[154:155]
	v_lshl_add_u64 v[158:159], v[154:155], 0, s[20:21]
	v_lshl_add_u64 v[164:165], v[158:159], 0, v[4:5]
	v_mov_b32_e32 v168, v202
	v_mov_b32_e32 v169, v203
	v_ashrrev_i32_e32 v157, 31, v156
	v_lshlrev_b64 v[156:157], 12, v[156:157]
	v_lshl_add_u64 v[156:157], s[14:15], 0, v[156:157]
	s_and_b64 vcc, exec, s[6:7]
	v_lshl_add_u64 v[156:157], v[4:5], 1, v[156:157]
	s_nop 1
	v_cvt_f32_ubyte0_e32 v165, v168
	v_cvt_f32_ubyte1_e32 v166, v168
	v_cvt_f32_ubyte2_e32 v167, v168
	v_cvt_f32_ubyte3_e32 v168, v168
	v_cvt_f32_ubyte0_e32 v3, v169
	v_cvt_f32_ubyte1_e32 v153, v169
	v_cvt_f32_ubyte2_e32 v163, v169
	v_cvt_f32_ubyte3_e32 v164, v169
	s_cbranch_vccnz .LBB0_764
	v_mul_f32_e32 v170, 0x3b808081, v166
	v_mul_f32_e32 v171, 0x3b808081, v167
	v_mul_f32_e32 v172, 0x3b808081, v168
	v_mul_f32_e32 v173, 0x3b808081, v3
	v_mul_f32_e32 v169, 0x3b808081, v165
	v_mul_f32_e32 v170, v59, v170
	v_mul_f32_e32 v171, v60, v171
	v_mul_f32_e32 v172, v61, v172
	v_mul_f32_e32 v173, v54, v173
	v_mul_f32_e32 v174, 0x3b808081, v153
	v_mul_f32_e32 v175, 0x3b808081, v163
	v_mul_f32_e32 v176, 0x3b808081, v164
	v_mul_f32_e32 v169, v58, v169
	v_mul_f32_e32 v174, v55, v174
	v_mul_f32_e32 v175, v56, v175
	v_mul_f32_e32 v176, v57, v176
	v_cvt_pk_bf16_f32 v170, v169, v170
	v_cvt_pk_bf16_f32 v171, v171, v172
	v_cvt_pk_bf16_f32 v172, v173, v174
	v_cvt_pk_bf16_f32 v173, v175, v176
	global_store_dwordx4 v[156:157], v[170:173], off
	s_cbranch_execnz .LBB0_734
.LBB0_733:
	s_nop 0
	v_lshl_add_u64 v[170:171], v[154:155], 0, v[4:5]
	v_add_co_u32_e32 v170, vcc, 0x2000, v170
	v_rcp_f32_e32 v172, v165
	s_nop 0
	v_addc_co_u32_e32 v171, vcc, 0, v171, vcc
	v_mov_b32_e32 v170, v234
	v_mov_b32_e32 v171, v235
	v_rcp_f32_e32 v173, v166
	v_rcp_f32_e32 v166, v167
	v_rcp_f32_e32 v167, v168
	v_rcp_f32_e32 v168, v3
	v_rcp_f32_e32 v169, v153
	v_rcp_f32_e32 v174, v163
	v_rcp_f32_e32 v175, v164
	s_nop 1
	v_cvt_f32_ubyte3_e32 v165, v170
	v_cvt_f32_ubyte2_e32 v164, v170
	v_cvt_f32_ubyte1_e32 v177, v170
	v_cvt_f32_ubyte0_e32 v176, v170
	v_cvt_f32_ubyte3_e32 v179, v171
	v_cvt_f32_ubyte2_e32 v178, v171
	v_cvt_f32_ubyte1_e32 v181, v171
	v_cvt_f32_ubyte0_e32 v180, v171
	v_pk_mul_f32 v[170:171], v[172:173], v[176:177]
	v_pk_mul_f32 v[164:165], v[166:167], v[164:165]
	v_pk_mul_f32 v[166:167], v[168:169], v[180:181]
	v_pk_mul_f32 v[168:169], v[174:175], v[178:179]
	v_pk_mul_f32 v[60:61], v[60:61], v[164:165]
	v_pk_mul_f32 v[58:59], v[58:59], v[170:171]
	v_pk_mul_f32 v[56:57], v[56:57], v[168:169]
	v_pk_mul_f32 v[54:55], v[54:55], v[166:167]
.LBB0_734:
	v_lshl_add_u64 v[158:159], v[158:159], 0, v[150:151]
	v_mov_b32_e32 v158, v204
	v_mov_b32_e32 v159, v205
	s_and_b64 vcc, exec, s[6:7]
	s_nop 1
	v_cvt_f32_ubyte0_e32 v163, v158
	v_cvt_f32_ubyte1_e32 v164, v158
	v_cvt_f32_ubyte2_e32 v165, v158
	v_cvt_f32_ubyte3_e32 v166, v158
	v_cvt_f32_ubyte0_e32 v3, v159
	v_cvt_f32_ubyte1_e32 v153, v159
	v_cvt_f32_ubyte2_e32 v158, v159
	v_cvt_f32_ubyte3_e32 v159, v159
	s_cbranch_vccnz .LBB0_765
	v_mul_f32_e32 v168, 0x3b808081, v164
	v_mul_f32_e32 v169, 0x3b808081, v165
	v_mul_f32_e32 v170, 0x3b808081, v166
	v_mul_f32_e32 v171, 0x3b808081, v3
	v_mul_f32_e32 v167, 0x3b808081, v163
	v_mul_f32_e32 v168, v27, v168
	v_mul_f32_e32 v169, v28, v169
	v_mul_f32_e32 v170, v29, v170
	v_mul_f32_e32 v171, v22, v171
	v_mul_f32_e32 v172, 0x3b808081, v153
	v_mul_f32_e32 v173, 0x3b808081, v158
	v_mul_f32_e32 v174, 0x3b808081, v159
	v_mul_f32_e32 v167, v26, v167
	v_mul_f32_e32 v172, v23, v172
	v_mul_f32_e32 v173, v24, v173
	v_mul_f32_e32 v174, v25, v174
	v_cvt_pk_bf16_f32 v168, v167, v168
	v_cvt_pk_bf16_f32 v169, v169, v170
	v_cvt_pk_bf16_f32 v170, v171, v172
	v_cvt_pk_bf16_f32 v171, v173, v174
	global_store_dwordx4 v[156:157], v[168:171], off offset:256
	s_cbranch_execnz .LBB0_737
.LBB0_736:
	v_lshl_add_u64 v[154:155], v[154:155], 0, v[150:151]
	v_add_co_u32_e32 v154, vcc, 0x2000, v154
	v_rcp_f32_e32 v156, v163
	s_nop 0
	v_addc_co_u32_e32 v155, vcc, 0, v155, vcc
	v_mov_b32_e32 v154, v236
	v_mov_b32_e32 v155, v237
	v_rcp_f32_e32 v157, v164
	v_rcp_f32_e32 v164, v165
	v_rcp_f32_e32 v165, v166
	v_rcp_f32_e32 v166, v3
	v_rcp_f32_e32 v167, v153
	v_rcp_f32_e32 v158, v158
	v_rcp_f32_e32 v159, v159
	s_nop 1
	v_cvt_f32_ubyte3_e32 v169, v154
	v_cvt_f32_ubyte2_e32 v168, v154
	v_cvt_f32_ubyte1_e32 v171, v154
	v_cvt_f32_ubyte0_e32 v170, v154
	v_cvt_f32_ubyte3_e32 v173, v155
	v_cvt_f32_ubyte2_e32 v172, v155
	v_cvt_f32_ubyte1_e32 v175, v155
	v_cvt_f32_ubyte0_e32 v174, v155
	v_pk_mul_f32 v[154:155], v[156:157], v[170:171]
	v_pk_mul_f32 v[156:157], v[164:165], v[168:169]
	v_pk_mul_f32 v[164:165], v[166:167], v[174:175]
	v_pk_mul_f32 v[158:159], v[158:159], v[172:173]
	v_pk_mul_f32 v[28:29], v[28:29], v[156:157]
	v_pk_mul_f32 v[26:27], v[26:27], v[154:155]
	v_pk_mul_f32 v[24:25], v[24:25], v[158:159]
	v_pk_mul_f32 v[22:23], v[22:23], v[164:165]
.LBB0_737:
	v_add_u32_e32 v156, 0xa0, v152
	v_mov_b64_e32 v[154:155], s[12:13]
	v_mad_i64_i32 v[154:155], s[30:31], v156, s63, v[154:155]
	v_lshl_add_u64 v[158:159], v[154:155], 0, s[20:21]
	v_lshl_add_u64 v[164:165], v[158:159], 0, v[4:5]
	v_mov_b32_e32 v168, v206
	v_mov_b32_e32 v169, v207
	v_ashrrev_i32_e32 v157, 31, v156
	v_lshlrev_b64 v[156:157], 12, v[156:157]
	v_lshl_add_u64 v[156:157], s[14:15], 0, v[156:157]
	s_and_b64 vcc, exec, s[6:7]
	v_lshl_add_u64 v[156:157], v[4:5], 1, v[156:157]
	s_nop 1
	v_cvt_f32_ubyte0_e32 v165, v168
	v_cvt_f32_ubyte1_e32 v166, v168
	v_cvt_f32_ubyte2_e32 v167, v168
	v_cvt_f32_ubyte3_e32 v168, v168
	v_cvt_f32_ubyte0_e32 v3, v169
	v_cvt_f32_ubyte1_e32 v153, v169
	v_cvt_f32_ubyte2_e32 v163, v169
	v_cvt_f32_ubyte3_e32 v164, v169
	s_cbranch_vccnz .LBB0_766
	v_mul_f32_e32 v170, 0x3b808081, v166
	v_mul_f32_e32 v171, 0x3b808081, v167
	v_mul_f32_e32 v172, 0x3b808081, v168
	v_mul_f32_e32 v173, 0x3b808081, v3
	v_mul_f32_e32 v169, 0x3b808081, v165
	v_mul_f32_e32 v170, v51, v170
	v_mul_f32_e32 v171, v52, v171
	v_mul_f32_e32 v172, v53, v172
	v_mul_f32_e32 v173, v46, v173
	v_mul_f32_e32 v174, 0x3b808081, v153
	v_mul_f32_e32 v175, 0x3b808081, v163
	v_mul_f32_e32 v176, 0x3b808081, v164
	v_mul_f32_e32 v169, v50, v169
	v_mul_f32_e32 v174, v47, v174
	v_mul_f32_e32 v175, v48, v175
	v_mul_f32_e32 v176, v49, v176
	v_cvt_pk_bf16_f32 v170, v169, v170
	v_cvt_pk_bf16_f32 v171, v171, v172
	v_cvt_pk_bf16_f32 v172, v173, v174
	v_cvt_pk_bf16_f32 v173, v175, v176
	global_store_dwordx4 v[156:157], v[170:173], off
	s_cbranch_execnz .LBB0_740
.LBB0_739:
	s_nop 0
	v_lshl_add_u64 v[170:171], v[154:155], 0, v[4:5]
	v_add_co_u32_e32 v170, vcc, 0x2000, v170
	v_rcp_f32_e32 v172, v165
	s_nop 0
	v_addc_co_u32_e32 v171, vcc, 0, v171, vcc
	v_mov_b32_e32 v170, v238
	v_mov_b32_e32 v171, v239
	v_rcp_f32_e32 v173, v166
	v_rcp_f32_e32 v166, v167
	v_rcp_f32_e32 v167, v168
	v_rcp_f32_e32 v168, v3
	v_rcp_f32_e32 v169, v153
	v_rcp_f32_e32 v174, v163
	v_rcp_f32_e32 v175, v164
	s_nop 1
	v_cvt_f32_ubyte3_e32 v165, v170
	v_cvt_f32_ubyte2_e32 v164, v170
	v_cvt_f32_ubyte1_e32 v177, v170
	v_cvt_f32_ubyte0_e32 v176, v170
	v_cvt_f32_ubyte3_e32 v179, v171
	v_cvt_f32_ubyte2_e32 v178, v171
	v_cvt_f32_ubyte1_e32 v181, v171
	v_cvt_f32_ubyte0_e32 v180, v171
	v_pk_mul_f32 v[170:171], v[172:173], v[176:177]
	v_pk_mul_f32 v[164:165], v[166:167], v[164:165]
	v_pk_mul_f32 v[166:167], v[168:169], v[180:181]
	v_pk_mul_f32 v[168:169], v[174:175], v[178:179]
	v_pk_mul_f32 v[52:53], v[52:53], v[164:165]
	v_pk_mul_f32 v[50:51], v[50:51], v[170:171]
	v_pk_mul_f32 v[48:49], v[48:49], v[168:169]
	v_pk_mul_f32 v[46:47], v[46:47], v[166:167]
.LBB0_740:
	v_lshl_add_u64 v[158:159], v[158:159], 0, v[150:151]
	v_mov_b32_e32 v158, v208
	v_mov_b32_e32 v159, v209
	s_and_b64 vcc, exec, s[6:7]
	s_nop 1
	v_cvt_f32_ubyte0_e32 v163, v158
	v_cvt_f32_ubyte1_e32 v164, v158
	v_cvt_f32_ubyte2_e32 v165, v158
	v_cvt_f32_ubyte3_e32 v166, v158
	v_cvt_f32_ubyte0_e32 v3, v159
	v_cvt_f32_ubyte1_e32 v153, v159
	v_cvt_f32_ubyte2_e32 v158, v159
	v_cvt_f32_ubyte3_e32 v159, v159
	s_cbranch_vccnz .LBB0_767
	v_mul_f32_e32 v168, 0x3b808081, v164
	v_mul_f32_e32 v169, 0x3b808081, v165
	v_mul_f32_e32 v170, 0x3b808081, v166
	v_mul_f32_e32 v171, 0x3b808081, v3
	v_mul_f32_e32 v167, 0x3b808081, v163
	v_mul_f32_e32 v168, v19, v168
	v_mul_f32_e32 v169, v20, v169
	v_mul_f32_e32 v170, v21, v170
	v_mul_f32_e32 v171, v14, v171
	v_mul_f32_e32 v172, 0x3b808081, v153
	v_mul_f32_e32 v173, 0x3b808081, v158
	v_mul_f32_e32 v174, 0x3b808081, v159
	v_mul_f32_e32 v167, v18, v167
	v_mul_f32_e32 v172, v15, v172
	v_mul_f32_e32 v173, v16, v173
	v_mul_f32_e32 v174, v17, v174
	v_cvt_pk_bf16_f32 v168, v167, v168
	v_cvt_pk_bf16_f32 v169, v169, v170
	v_cvt_pk_bf16_f32 v170, v171, v172
	v_cvt_pk_bf16_f32 v171, v173, v174
	global_store_dwordx4 v[156:157], v[168:171], off offset:256
	s_cbranch_execnz .LBB0_743
.LBB0_742:
	v_lshl_add_u64 v[154:155], v[154:155], 0, v[150:151]
	v_add_co_u32_e32 v154, vcc, 0x2000, v154
	v_rcp_f32_e32 v156, v163
	s_nop 0
	v_addc_co_u32_e32 v155, vcc, 0, v155, vcc
	v_mov_b32_e32 v154, v240
	v_mov_b32_e32 v155, v241
	v_rcp_f32_e32 v157, v164
	v_rcp_f32_e32 v164, v165
	v_rcp_f32_e32 v165, v166
	v_rcp_f32_e32 v166, v3
	v_rcp_f32_e32 v167, v153
	v_rcp_f32_e32 v158, v158
	v_rcp_f32_e32 v159, v159
	s_nop 1
	v_cvt_f32_ubyte3_e32 v169, v154
	v_cvt_f32_ubyte2_e32 v168, v154
	v_cvt_f32_ubyte1_e32 v171, v154
	v_cvt_f32_ubyte0_e32 v170, v154
	v_cvt_f32_ubyte3_e32 v173, v155
	v_cvt_f32_ubyte2_e32 v172, v155
	v_cvt_f32_ubyte1_e32 v175, v155
	v_cvt_f32_ubyte0_e32 v174, v155
	v_pk_mul_f32 v[154:155], v[156:157], v[170:171]
	v_pk_mul_f32 v[156:157], v[164:165], v[168:169]
	v_pk_mul_f32 v[164:165], v[166:167], v[174:175]
	v_pk_mul_f32 v[158:159], v[158:159], v[172:173]
	v_pk_mul_f32 v[20:21], v[20:21], v[156:157]
	v_pk_mul_f32 v[18:19], v[18:19], v[154:155]
	v_pk_mul_f32 v[16:17], v[16:17], v[158:159]
	v_pk_mul_f32 v[14:15], v[14:15], v[164:165]
.LBB0_743:
	v_add_u32_e32 v154, 0xb0, v152
	v_mov_b64_e32 v[152:153], s[12:13]
	v_mad_i64_i32 v[152:153], s[30:31], v154, s63, v[152:153]
	v_lshl_add_u64 v[156:157], v[152:153], 0, s[20:21]
	v_lshl_add_u64 v[158:159], v[156:157], 0, v[4:5]
	v_mov_b32_e32 v168, v210
	v_mov_b32_e32 v169, v211
	v_ashrrev_i32_e32 v155, 31, v154
	v_lshlrev_b64 v[154:155], 12, v[154:155]
	v_lshl_add_u64 v[154:155], s[14:15], 0, v[154:155]
	s_and_b64 vcc, exec, s[6:7]
	v_lshl_add_u64 v[154:155], v[4:5], 1, v[154:155]
	s_nop 1
	v_cvt_f32_ubyte0_e32 v164, v168
	v_cvt_f32_ubyte1_e32 v165, v168
	v_cvt_f32_ubyte2_e32 v166, v168
	v_cvt_f32_ubyte3_e32 v167, v168
	v_cvt_f32_ubyte0_e32 v3, v169
	v_cvt_f32_ubyte1_e32 v158, v169
	v_cvt_f32_ubyte2_e32 v159, v169
	v_cvt_f32_ubyte3_e32 v163, v169
	s_cbranch_vccnz .LBB0_768
	v_mul_f32_e32 v168, 0x3b808081, v164
	v_mul_f32_e32 v169, 0x3b808081, v165
	v_mul_f32_e32 v170, 0x3b808081, v166
	v_mul_f32_e32 v171, 0x3b808081, v167
	v_mul_f32_e32 v168, v42, v168
	v_mul_f32_e32 v169, v43, v169
	v_mul_f32_e32 v170, v44, v170
	v_mul_f32_e32 v171, v45, v171
	v_mul_f32_e32 v172, 0x3b808081, v3
	v_mul_f32_e32 v173, 0x3b808081, v158
	v_mul_f32_e32 v174, 0x3b808081, v159
	v_mul_f32_e32 v175, 0x3b808081, v163
	v_mul_f32_e32 v172, v38, v172
	v_mul_f32_e32 v173, v39, v173
	v_mul_f32_e32 v174, v40, v174
	v_mul_f32_e32 v175, v41, v175
	v_cvt_pk_bf16_f32 v168, v168, v169
	v_cvt_pk_bf16_f32 v169, v170, v171
	v_cvt_pk_bf16_f32 v170, v172, v173
	v_cvt_pk_bf16_f32 v171, v174, v175
	global_store_dwordx4 v[154:155], v[168:171], off
	s_cbranch_execnz .LBB0_746
.LBB0_745:
	v_lshl_add_u64 v[4:5], v[152:153], 0, v[4:5]
	v_add_co_u32_e32 v4, vcc, 0x2000, v4
	v_rcp_f32_e32 v164, v164
	s_nop 0
	v_addc_co_u32_e32 v5, vcc, 0, v5, vcc
	v_mov_b32_e32 v4, v242
	v_mov_b32_e32 v5, v243
	v_rcp_f32_e32 v165, v165
	v_rcp_f32_e32 v166, v166
	v_rcp_f32_e32 v167, v167
	v_rcp_f32_e32 v168, v3
	v_rcp_f32_e32 v169, v158
	v_rcp_f32_e32 v158, v159
	v_rcp_f32_e32 v159, v163
	s_nop 1
	v_cvt_f32_ubyte3_e32 v171, v4
	v_cvt_f32_ubyte2_e32 v170, v4
	v_cvt_f32_ubyte1_e32 v173, v4
	v_cvt_f32_ubyte0_e32 v172, v4
	v_cvt_f32_ubyte3_e32 v175, v5
	v_cvt_f32_ubyte2_e32 v174, v5
	v_cvt_f32_ubyte1_e32 v177, v5
	v_cvt_f32_ubyte0_e32 v176, v5
	v_pk_mul_f32 v[4:5], v[164:165], v[172:173]
	v_pk_mul_f32 v[164:165], v[166:167], v[170:171]
	v_pk_mul_f32 v[166:167], v[168:169], v[176:177]
	v_pk_mul_f32 v[158:159], v[158:159], v[174:175]
	v_pk_mul_f32 v[44:45], v[44:45], v[164:165]
	v_pk_mul_f32 v[42:43], v[42:43], v[4:5]
	v_pk_mul_f32 v[40:41], v[40:41], v[158:159]
	v_pk_mul_f32 v[38:39], v[38:39], v[166:167]
.LBB0_746:
	v_lshl_add_u64 v[4:5], v[156:157], 0, v[150:151]
	v_mov_b32_e32 v164, v212
	v_mov_b32_e32 v165, v213
	s_and_b64 vcc, exec, s[6:7]
	s_nop 1
	v_cvt_f32_ubyte0_e32 v157, v164
	v_cvt_f32_ubyte1_e32 v158, v164
	v_cvt_f32_ubyte2_e32 v159, v164
	v_cvt_f32_ubyte3_e32 v163, v164
	v_cvt_f32_ubyte0_e32 v3, v165
	v_cvt_f32_ubyte1_e32 v4, v165
	v_cvt_f32_ubyte2_e32 v5, v165
	v_cvt_f32_ubyte3_e32 v156, v165
	s_cbranch_vccnz .LBB0_769
	v_mul_f32_e32 v164, 0x3b808081, v157
	v_mul_f32_e32 v165, 0x3b808081, v158
	v_mul_f32_e32 v166, 0x3b808081, v159
	v_mul_f32_e32 v167, 0x3b808081, v163
	v_mul_f32_e32 v164, v10, v164
	v_mul_f32_e32 v165, v11, v165
	v_mul_f32_e32 v166, v12, v166
	v_mul_f32_e32 v167, v13, v167
	v_mul_f32_e32 v168, 0x3b808081, v3
	v_mul_f32_e32 v169, 0x3b808081, v4
	v_mul_f32_e32 v170, 0x3b808081, v5
	v_mul_f32_e32 v171, 0x3b808081, v156
	v_mul_f32_e32 v168, v6, v168
	v_mul_f32_e32 v169, v7, v169
	v_mul_f32_e32 v170, v8, v170
	v_mul_f32_e32 v171, v9, v171
	v_cvt_pk_bf16_f32 v164, v164, v165
	v_cvt_pk_bf16_f32 v165, v166, v167
	v_cvt_pk_bf16_f32 v166, v168, v169
	v_cvt_pk_bf16_f32 v167, v170, v171
	global_store_dwordx4 v[154:155], v[164:167], off offset:256
	s_cbranch_execnz .LBB0_749
.LBB0_748:
	v_lshl_add_u64 v[150:151], v[152:153], 0, v[150:151]
	v_add_co_u32_e32 v150, vcc, 0x2000, v150
	v_rcp_f32_e32 v152, v157
	s_nop 0
	v_addc_co_u32_e32 v151, vcc, 0, v151, vcc
	v_mov_b32_e32 v150, v244
	v_mov_b32_e32 v151, v245
	v_rcp_f32_e32 v153, v158
	v_rcp_f32_e32 v154, v159
	v_rcp_f32_e32 v155, v163
	v_rcp_f32_e32 v158, v3
	v_rcp_f32_e32 v159, v4
	v_rcp_f32_e32 v4, v5
	v_rcp_f32_e32 v5, v156
	s_nop 1
	v_cvt_f32_ubyte3_e32 v157, v150
	v_cvt_f32_ubyte2_e32 v156, v150
	v_cvt_f32_ubyte1_e32 v165, v150
	v_cvt_f32_ubyte0_e32 v164, v150
	v_cvt_f32_ubyte3_e32 v167, v151
	v_cvt_f32_ubyte2_e32 v166, v151
	v_cvt_f32_ubyte1_e32 v169, v151
	v_cvt_f32_ubyte0_e32 v168, v151
	v_pk_mul_f32 v[150:151], v[152:153], v[164:165]
	v_pk_mul_f32 v[152:153], v[154:155], v[156:157]
	v_pk_mul_f32 v[154:155], v[158:159], v[168:169]
	v_pk_mul_f32 v[4:5], v[4:5], v[166:167]
	v_pk_mul_f32 v[12:13], v[12:13], v[152:153]
	v_pk_mul_f32 v[10:11], v[10:11], v[150:151]
	v_pk_mul_f32 v[8:9], v[8:9], v[4:5]
	v_pk_mul_f32 v[6:7], v[6:7], v[154:155]
